# fp8 GEMM K-loops: the second sub-phase of a tile's first K iteration also runs an out-of-line copy whose MFMAs take the inline constant 0 as C, so no zeroing moves remain anywhere
# baseline (speedup 1.0000x reference)
.Llzf_2:
	v_mfma_f32_16x16x128_f8f6f4 v[126:129], v[130:137], v[186:193], 0
	v_mfma_f32_16x16x128_f8f6f4 v[122:125], v[138:145], v[186:193], 0
	v_mfma_f32_16x16x128_f8f6f4 v[110:113], v[130:137], v[194:201], 0
	v_mfma_f32_16x16x128_f8f6f4 v[106:109], v[138:145], v[194:201], 0
	v_mfma_f32_16x16x128_f8f6f4 v[98:101], v[130:137], v[202:209], 0
	v_mfma_f32_16x16x128_f8f6f4 v[162:165], v[138:145], v[202:209], 0
	v_mfma_f32_16x16x128_f8f6f4 v[172:175], v[130:137], v[210:217], 0
	v_mfma_f32_16x16x128_f8f6f4 v[218:221], v[138:145], v[210:217], 0
	s_setprio 0
	s_setprio 1
	v_mfma_f32_16x16x128_f8f6f4 v[118:121], v[146:153], v[186:193], 0
	v_mfma_f32_16x16x128_f8f6f4 v[114:117], v[154:161], v[186:193], 0
	v_mfma_f32_16x16x128_f8f6f4 v[102:105], v[146:153], v[194:201], 0
	v_mfma_f32_16x16x128_f8f6f4 v[186:189], v[154:161], v[194:201], 0
	v_mfma_f32_16x16x128_f8f6f4 v[190:193], v[146:153], v[202:209], 0
	v_mfma_f32_16x16x128_f8f6f4 v[194:197], v[154:161], v[202:209], 0
	v_mfma_f32_16x16x128_f8f6f4 v[198:201], v[146:153], v[210:217], 0
	v_mfma_f32_16x16x128_f8f6f4 v[202:205], v[154:161], v[210:217], 0
	s_branch .Llzj_2
.Llzg_2:
	v_mfma_f32_16x16x128_f8f6f4 v[62:65], v[130:137], v[66:73], 0
	v_mfma_f32_16x16x128_f8f6f4 v[58:61], v[138:145], v[66:73], 0
	v_mfma_f32_16x16x128_f8f6f4 v[50:53], v[130:137], v[74:81], 0
	v_mfma_f32_16x16x128_f8f6f4 v[206:209], v[138:145], v[74:81], 0
	v_mfma_f32_16x16x128_f8f6f4 v[210:213], v[130:137], v[82:89], 0
	v_mfma_f32_16x16x128_f8f6f4 v[214:217], v[138:145], v[82:89], 0
	v_mfma_f32_16x16x128_f8f6f4 v[244:247], v[130:137], v[90:97], 0
	v_mfma_f32_16x16x128_f8f6f4 v[248:251], v[138:145], v[90:97], 0
	s_setprio 0
	s_setprio 1
	v_mfma_f32_16x16x128_f8f6f4 v[54:57], v[146:153], v[66:73], 0
	v_mfma_f32_16x16x128_f8f6f4 v[234:237], v[154:161], v[66:73], 0
	v_mfma_f32_16x16x128_f8f6f4 v[176:179], v[146:153], v[74:81], 0
	v_mfma_f32_16x16x128_f8f6f4 v[180:183], v[154:161], v[74:81], 0
	v_mfma_f32_16x16x128_f8f6f4 v[226:229], v[146:153], v[82:89], 0
	v_mfma_f32_16x16x128_f8f6f4 v[230:233], v[154:161], v[82:89], 0
	v_mfma_f32_16x16x128_f8f6f4 v[222:225], v[146:153], v[90:97], 0
	v_mfma_f32_16x16x128_f8f6f4 v[238:241], v[154:161], v[90:97], 0
	s_branch .Llzk_2

.Llzj_2:
	s_setprio 0
	s_barrier
	v_mov_b32_e32 v0, v166
	s_mov_b32 m0, s37
	s_nop 2
	ds_read_b128 v[66:69], v171 offset:16384
	ds_read_b128 v[70:73], v171 offset:17408
	ds_read_b128 v[74:77], v171 offset:18432
	ds_read_b128 v[78:81], v171 offset:19456
	ds_read_b128 v[82:85], v171 offset:20480
	ds_read_b128 v[86:89], v171 offset:21504
	ds_read_b128 v[90:93], v171 offset:22528
	ds_read_b128 v[94:97], v171 offset:23552
	s_add_u32 s62, s26, 0x20000
	global_load_lds_dwordx4 v0, s[26:27]
	v_mov_b32_e32 v0, v168
	s_mov_b32 m0, s38
	s_addc_u32 s63, s27, 0
	global_load_lds_dwordx4 v0, s[26:27]
	v_mov_b32_e32 v0, v166
	s_mov_b32 m0, s40
	s_nop 0
	global_load_lds_dwordx4 v0, s[62:63]
	v_mov_b32_e32 v0, v168
	s_mov_b32 m0, s41
	s_nop 0
	global_load_lds_dwordx4 v0, s[62:63]
	v_mov_b32_e32 v0, v167
	s_mov_b32 m0, s42
	s_nop 0
	global_load_lds_dwordx4 v0, s[24:25]
	v_mov_b32_e32 v0, v169
	s_mov_b32 m0, s43
	s_nop 0
	global_load_lds_dwordx4 v0, s[24:25]
	s_waitcnt vmcnt(8)
	s_waitcnt lgkmcnt(0)
	s_barrier
	s_setprio 1
	s_waitcnt lgkmcnt(0)
	s_cmp_eq_u32 s61, -2
	s_cbranch_scc1 .Llzg_2
	v_mfma_f32_16x16x128_f8f6f4 v[62:65], v[130:137], v[66:73], v[62:65]
	v_mfma_f32_16x16x128_f8f6f4 v[58:61], v[138:145], v[66:73], v[58:61]
	v_mfma_f32_16x16x128_f8f6f4 v[50:53], v[130:137], v[74:81], v[50:53]
	v_mfma_f32_16x16x128_f8f6f4 v[206:209], v[138:145], v[74:81], v[42:45]
	v_mfma_f32_16x16x128_f8f6f4 v[210:213], v[130:137], v[82:89], v[34:37]
	v_mfma_f32_16x16x128_f8f6f4 v[214:217], v[138:145], v[82:89], v[26:29]
	v_mfma_f32_16x16x128_f8f6f4 v[244:247], v[130:137], v[90:97], v[18:21]
	v_mfma_f32_16x16x128_f8f6f4 v[248:251], v[138:145], v[90:97], v[10:13]
	s_setprio 0
	s_setprio 1
	v_mfma_f32_16x16x128_f8f6f4 v[54:57], v[146:153], v[66:73], v[54:57]
	v_mfma_f32_16x16x128_f8f6f4 v[234:237], v[154:161], v[66:73], v[46:49]
	v_mfma_f32_16x16x128_f8f6f4 v[176:179], v[146:153], v[74:81], v[38:41]
	v_mfma_f32_16x16x128_f8f6f4 v[180:183], v[154:161], v[74:81], v[30:33]
	v_mfma_f32_16x16x128_f8f6f4 v[226:229], v[146:153], v[82:89], v[22:25]
	v_mfma_f32_16x16x128_f8f6f4 v[230:233], v[154:161], v[82:89], v[14:17]
	v_mfma_f32_16x16x128_f8f6f4 v[222:225], v[146:153], v[90:97], v[6:9]
	v_mfma_f32_16x16x128_f8f6f4 v[238:241], v[154:161], v[90:97], v[2:5]
.Llzk_2:
	s_setprio 0
	s_barrier
	v_add_u32_e32 v0, s48, v170
	s_nop 3
	ds_read_b128 v[2:5], v0
	ds_read_b128 v[6:9], v0 offset:1024
	ds_read_b128 v[10:13], v0 offset:2048
	ds_read_b128 v[14:17], v0 offset:3072
	v_add_u32_e32 v0, s53, v170
	ds_read_b128 v[130:133], v0
	ds_read_b128 v[134:137], v0 offset:1024
	ds_read_b128 v[138:141], v0 offset:2048
	ds_read_b128 v[142:145], v0 offset:3072
	v_mov_b32_e32 v0, v167
	ds_read_b128 v[18:21], v171 offset:32768
	ds_read_b128 v[22:25], v171 offset:33792
	ds_read_b128 v[26:29], v171 offset:34816
	ds_read_b128 v[30:33], v171 offset:35840
	ds_read_b128 v[34:37], v171 offset:36864
	ds_read_b128 v[38:41], v171 offset:37888
	ds_read_b128 v[42:45], v171 offset:38912
	ds_read_b128 v[46:49], v171 offset:39936
	s_mov_b32 m0, s44
	v_add_u32_e32 v0, 0x20000, v0
	global_load_lds_dwordx4 v0, s[24:25]
	v_mov_b32_e32 v0, v169
	s_mov_b32 m0, s45
	v_add_u32_e32 v0, 0x20000, v0
	global_load_lds_dwordx4 v0, s[24:25]
	s_waitcnt vmcnt(8)
	s_waitcnt lgkmcnt(0)
	s_barrier
	s_setprio 1
	s_waitcnt lgkmcnt(0)
	v_mfma_f32_16x16x128_f8f6f4 v[126:129], v[2:9], v[18:25], v[126:129]
	v_mfma_f32_16x16x128_f8f6f4 v[122:125], v[10:17], v[18:25], v[122:125]
	v_mfma_f32_16x16x128_f8f6f4 v[110:113], v[2:9], v[26:33], v[110:113]
	v_mfma_f32_16x16x128_f8f6f4 v[106:109], v[10:17], v[26:33], v[106:109]
	v_mfma_f32_16x16x128_f8f6f4 v[98:101], v[2:9], v[34:41], v[98:101]
	v_mfma_f32_16x16x128_f8f6f4 v[90:93], v[10:17], v[34:41], v[162:165]
	v_mfma_f32_16x16x128_f8f6f4 v[82:85], v[2:9], v[42:49], v[172:175]
	v_mfma_f32_16x16x128_f8f6f4 v[74:77], v[10:17], v[42:49], v[218:221]
	s_setprio 0
	s_setprio 1
	v_mfma_f32_16x16x128_f8f6f4 v[118:121], v[130:137], v[18:25], v[118:121]
	v_mfma_f32_16x16x128_f8f6f4 v[114:117], v[138:145], v[18:25], v[114:117]
	v_mfma_f32_16x16x128_f8f6f4 v[102:105], v[130:137], v[26:33], v[102:105]
	v_mfma_f32_16x16x128_f8f6f4 v[94:97], v[138:145], v[26:33], v[186:189]
	v_mfma_f32_16x16x128_f8f6f4 v[86:89], v[130:137], v[34:41], v[190:193]
	v_mfma_f32_16x16x128_f8f6f4 v[78:81], v[138:145], v[34:41], v[194:197]
	v_mfma_f32_16x16x128_f8f6f4 v[70:73], v[130:137], v[42:49], v[198:201]
	v_mfma_f32_16x16x128_f8f6f4 v[66:69], v[138:145], v[42:49], v[202:205]
	s_setprio 0
	s_barrier
	v_mov_b32_e32 v0, v166
	ds_read_b128 v[146:149], v171 offset:49152
	ds_read_b128 v[150:153], v171 offset:50176
	ds_read_b128 v[154:157], v171 offset:51200
	ds_read_b128 v[158:161], v171 offset:52224
	ds_read_b128 v[186:189], v171 offset:53248
	ds_read_b128 v[190:193], v171 offset:54272
	ds_read_b128 v[194:197], v171 offset:55296
	ds_read_b128 v[198:201], v171 offset:56320
	s_mov_b32 m0, s49
	v_lshl_add_u64 v[18:19], s[26:27], 0, v[0:1]
	v_lshl_add_u64 v[18:19], v[18:19], 0, s[82:83]
	v_mov_b32_e32 v0, v168
	global_load_lds_dwordx4 v[18:19], off
	s_mov_b32 m0, s50
	v_lshl_add_u64 v[18:19], s[26:27], 0, v[0:1]
	v_lshl_add_u64 v[18:19], v[18:19], 0, s[82:83]
	s_add_u32 s26, s26, 0x20080
	v_mov_b32_e32 v0, v166
	global_load_lds_dwordx4 v[18:19], off
	s_addc_u32 s27, s27, 0
	s_mov_b32 m0, s54
	s_nop 0
	global_load_lds_dwordx4 v0, s[26:27]
	v_mov_b32_e32 v0, v168
	s_mov_b32 m0, s55
	s_nop 0
	global_load_lds_dwordx4 v0, s[26:27]
	v_mov_b32_e32 v0, v167
	s_mov_b32 m0, s51
	v_lshl_add_u64 v[18:19], s[24:25], 0, v[0:1]
	v_lshl_add_u64 v[18:19], v[18:19], 0, s[82:83]
	v_mov_b32_e32 v0, v169
	global_load_lds_dwordx4 v[18:19], off
	s_mov_b32 m0, s52
	v_lshl_add_u64 v[18:19], s[24:25], 0, v[0:1]
	v_lshl_add_u64 v[18:19], v[18:19], 0, s[82:83]
	global_load_lds_dwordx4 v[18:19], off
	s_waitcnt vmcnt(8)
	s_waitcnt lgkmcnt(0)
	s_barrier
	s_setprio 1
	s_waitcnt lgkmcnt(0)
	v_mfma_f32_16x16x128_f8f6f4 v[62:65], v[2:9], v[146:153], v[62:65]
	v_mfma_f32_16x16x128_f8f6f4 v[58:61], v[10:17], v[146:153], v[58:61]
	v_mfma_f32_16x16x128_f8f6f4 v[50:53], v[2:9], v[154:161], v[50:53]
	v_mfma_f32_16x16x128_f8f6f4 v[42:45], v[10:17], v[154:161], v[206:209]
	v_mfma_f32_16x16x128_f8f6f4 v[34:37], v[2:9], v[186:193], v[210:213]
	v_mfma_f32_16x16x128_f8f6f4 v[26:29], v[10:17], v[186:193], v[214:217]
	v_mfma_f32_16x16x128_f8f6f4 v[18:21], v[2:9], v[194:201], v[244:247]
	v_mfma_f32_16x16x128_f8f6f4 v[10:13], v[10:17], v[194:201], v[248:251]
	s_setprio 0
	s_setprio 1
	v_mfma_f32_16x16x128_f8f6f4 v[54:57], v[130:137], v[146:153], v[54:57]
	v_mfma_f32_16x16x128_f8f6f4 v[46:49], v[138:145], v[146:153], v[234:237]
	v_mfma_f32_16x16x128_f8f6f4 v[38:41], v[130:137], v[154:161], v[176:179]
	v_mfma_f32_16x16x128_f8f6f4 v[30:33], v[138:145], v[154:161], v[180:183]
	v_mfma_f32_16x16x128_f8f6f4 v[22:25], v[130:137], v[186:193], v[226:229]
	v_mfma_f32_16x16x128_f8f6f4 v[14:17], v[138:145], v[186:193], v[230:233]
	v_mfma_f32_16x16x128_f8f6f4 v[6:9], v[130:137], v[194:201], v[222:225]
	v_mfma_f32_16x16x128_f8f6f4 v[2:5], v[138:145], v[194:201], v[238:241]
	s_setprio 0
	s_barrier
	s_add_i32 s61, s61, 2
	s_add_u32 s59, s59, 0x100
	s_addc_u32 s60, s60, 0
	s_add_u32 s22, s22, 0x100
	s_addc_u32 s23, s23, 0
	s_cmp_gt_u32 s61, 5
	s_cbranch_scc0 .LBB0_546
	s_and_b64 vcc, exec, s[10:11]
	s_cbranch_vccz .LBB0_549
	s_barrier

.Llzf_3:
	v_mfma_f32_16x16x128_f8f6f4 v[126:129], v[138:145], v[170:177], 0
	v_mfma_f32_16x16x128_f8f6f4 v[122:125], v[146:153], v[170:177], 0
	v_mfma_f32_16x16x128_f8f6f4 v[118:121], v[138:145], v[186:193], 0
	v_mfma_f32_16x16x128_f8f6f4 v[110:113], v[146:153], v[186:193], 0
	v_mfma_f32_16x16x128_f8f6f4 v[102:105], v[138:145], v[194:201], 0
	v_mfma_f32_16x16x128_f8f6f4 v[178:181], v[146:153], v[194:201], 0
	v_mfma_f32_16x16x128_f8f6f4 v[210:213], v[138:145], v[202:209], 0
	v_mfma_f32_16x16x128_f8f6f4 v[214:217], v[146:153], v[202:209], 0
	s_setprio 0
	s_setprio 1
	v_mfma_f32_16x16x128_f8f6f4 v[114:117], v[154:161], v[170:177], 0
	v_mfma_f32_16x16x128_f8f6f4 v[106:109], v[162:169], v[170:177], 0
	v_mfma_f32_16x16x128_f8f6f4 v[98:101], v[154:161], v[186:193], 0
	v_mfma_f32_16x16x128_f8f6f4 v[170:173], v[162:169], v[186:193], 0
	v_mfma_f32_16x16x128_f8f6f4 v[174:177], v[154:161], v[194:201], 0
	v_mfma_f32_16x16x128_f8f6f4 v[186:189], v[162:169], v[194:201], 0
	v_mfma_f32_16x16x128_f8f6f4 v[190:193], v[154:161], v[202:209], 0
	v_mfma_f32_16x16x128_f8f6f4 v[194:197], v[162:169], v[202:209], 0
	s_branch .Llzj_3
.Llzg_3:
	v_mfma_f32_16x16x128_f8f6f4 v[62:65], v[138:145], v[66:73], 0
	v_mfma_f32_16x16x128_f8f6f4 v[58:61], v[146:153], v[66:73], 0
	v_mfma_f32_16x16x128_f8f6f4 v[54:57], v[138:145], v[74:81], 0
	v_mfma_f32_16x16x128_f8f6f4 v[198:201], v[146:153], v[74:81], 0
	v_mfma_f32_16x16x128_f8f6f4 v[202:205], v[138:145], v[82:89], 0
	v_mfma_f32_16x16x128_f8f6f4 v[206:209], v[146:153], v[82:89], 0
	v_mfma_f32_16x16x128_f8f6f4 v[218:221], v[138:145], v[90:97], 0
	v_mfma_f32_16x16x128_f8f6f4 v[222:225], v[146:153], v[90:97], 0
	s_setprio 0
	s_setprio 1
	v_mfma_f32_16x16x128_f8f6f4 v[50:53], v[154:161], v[66:73], 0
	v_mfma_f32_16x16x128_f8f6f4 v[226:229], v[162:169], v[66:73], 0
	v_mfma_f32_16x16x128_f8f6f4 v[230:233], v[154:161], v[74:81], 0
	v_mfma_f32_16x16x128_f8f6f4 v[234:237], v[162:169], v[74:81], 0
	v_mfma_f32_16x16x128_f8f6f4 v[238:241], v[154:161], v[82:89], 0
	v_mfma_f32_16x16x128_f8f6f4 v[244:247], v[162:169], v[82:89], 0
	v_mfma_f32_16x16x128_f8f6f4 v[248:251], v[154:161], v[90:97], 0
	v_mfma_f32_16x16x128_f8f6f4 v[182:185], v[162:169], v[90:97], 0
	s_branch .Llzk_3

.Llzj_3:
	s_setprio 0
	s_barrier
	v_mov_b32_e32 v0, v132
	s_mov_b32 m0, s31
	s_nop 2
	ds_read_b128 v[66:69], v137 offset:16384
	ds_read_b128 v[70:73], v137 offset:17408
	ds_read_b128 v[74:77], v137 offset:18432
	ds_read_b128 v[78:81], v137 offset:19456
	ds_read_b128 v[82:85], v137 offset:20480
	ds_read_b128 v[86:89], v137 offset:21504
	ds_read_b128 v[90:93], v137 offset:22528
	ds_read_b128 v[94:97], v137 offset:23552
	s_add_u32 s60, s24, 0x20000
	global_load_lds_dwordx4 v0, s[24:25]
	v_mov_b32_e32 v0, v134
	s_mov_b32 m0, s33
	s_addc_u32 s61, s25, 0
	global_load_lds_dwordx4 v0, s[24:25]
	v_mov_b32_e32 v0, v132
	s_mov_b32 m0, s35
	s_nop 0
	global_load_lds_dwordx4 v0, s[60:61]
	v_mov_b32_e32 v0, v134
	s_mov_b32 m0, s36
	s_nop 0
	global_load_lds_dwordx4 v0, s[60:61]
	v_mov_b32_e32 v0, v133
	s_mov_b32 m0, s37
	s_nop 0
	global_load_lds_dwordx4 v0, s[22:23]
	v_mov_b32_e32 v0, v135
	s_mov_b32 m0, s38
	s_nop 0
	global_load_lds_dwordx4 v0, s[22:23]
	s_waitcnt vmcnt(8)
	s_waitcnt lgkmcnt(0)
	s_barrier
	s_setprio 1
	s_waitcnt lgkmcnt(0)
	s_cmp_eq_u32 s58, -2
	s_cbranch_scc1 .Llzg_3
	v_mfma_f32_16x16x128_f8f6f4 v[62:65], v[138:145], v[66:73], v[62:65]
	v_mfma_f32_16x16x128_f8f6f4 v[58:61], v[146:153], v[66:73], v[58:61]
	v_mfma_f32_16x16x128_f8f6f4 v[54:57], v[138:145], v[74:81], v[54:57]
	v_mfma_f32_16x16x128_f8f6f4 v[198:201], v[146:153], v[74:81], v[46:49]
	v_mfma_f32_16x16x128_f8f6f4 v[202:205], v[138:145], v[82:89], v[38:41]
	v_mfma_f32_16x16x128_f8f6f4 v[206:209], v[146:153], v[82:89], v[30:33]
	v_mfma_f32_16x16x128_f8f6f4 v[218:221], v[138:145], v[90:97], v[22:25]
	v_mfma_f32_16x16x128_f8f6f4 v[222:225], v[146:153], v[90:97], v[14:17]
	s_setprio 0
	s_setprio 1
	v_mfma_f32_16x16x128_f8f6f4 v[50:53], v[154:161], v[66:73], v[50:53]
	v_mfma_f32_16x16x128_f8f6f4 v[226:229], v[162:169], v[66:73], v[42:45]
	v_mfma_f32_16x16x128_f8f6f4 v[230:233], v[154:161], v[74:81], v[34:37]
	v_mfma_f32_16x16x128_f8f6f4 v[234:237], v[162:169], v[74:81], v[26:29]
	v_mfma_f32_16x16x128_f8f6f4 v[238:241], v[154:161], v[82:89], v[18:21]
	v_mfma_f32_16x16x128_f8f6f4 v[244:247], v[162:169], v[82:89], v[10:13]
	v_mfma_f32_16x16x128_f8f6f4 v[248:251], v[154:161], v[90:97], v[6:9]
	v_mfma_f32_16x16x128_f8f6f4 v[182:185], v[162:169], v[90:97], v[2:5]
.Llzk_3:
	s_setprio 0
	s_barrier
	v_add_u32_e32 v0, s43, v136
	s_nop 3
	ds_read_b128 v[2:5], v0
	ds_read_b128 v[6:9], v0 offset:1024
	ds_read_b128 v[10:13], v0 offset:2048
	ds_read_b128 v[14:17], v0 offset:3072
	v_add_u32_e32 v0, s48, v136
	ds_read_b128 v[138:141], v0
	ds_read_b128 v[142:145], v0 offset:1024
	ds_read_b128 v[146:149], v0 offset:2048
	ds_read_b128 v[150:153], v0 offset:3072
	v_mov_b32_e32 v0, v133
	ds_read_b128 v[18:21], v137 offset:32768
	ds_read_b128 v[22:25], v137 offset:33792
	ds_read_b128 v[26:29], v137 offset:34816
	ds_read_b128 v[30:33], v137 offset:35840
	ds_read_b128 v[34:37], v137 offset:36864
	ds_read_b128 v[38:41], v137 offset:37888
	ds_read_b128 v[42:45], v137 offset:38912
	ds_read_b128 v[46:49], v137 offset:39936
	s_mov_b32 m0, s39
	v_add_u32_e32 v0, 0x20000, v0
	global_load_lds_dwordx4 v0, s[22:23]
	v_mov_b32_e32 v0, v135
	s_mov_b32 m0, s40
	v_add_u32_e32 v0, 0x20000, v0
	global_load_lds_dwordx4 v0, s[22:23]
	s_waitcnt vmcnt(8)
	s_waitcnt lgkmcnt(0)
	s_barrier
	s_setprio 1
	s_waitcnt lgkmcnt(0)
	v_mfma_f32_16x16x128_f8f6f4 v[126:129], v[2:9], v[18:25], v[126:129]
	v_mfma_f32_16x16x128_f8f6f4 v[122:125], v[10:17], v[18:25], v[122:125]
	v_mfma_f32_16x16x128_f8f6f4 v[118:121], v[2:9], v[26:33], v[118:121]
	v_mfma_f32_16x16x128_f8f6f4 v[110:113], v[10:17], v[26:33], v[110:113]
	v_mfma_f32_16x16x128_f8f6f4 v[102:105], v[2:9], v[34:41], v[102:105]
	v_mfma_f32_16x16x128_f8f6f4 v[94:97], v[10:17], v[34:41], v[178:181]
	v_mfma_f32_16x16x128_f8f6f4 v[86:89], v[2:9], v[42:49], v[210:213]
	v_mfma_f32_16x16x128_f8f6f4 v[78:81], v[10:17], v[42:49], v[214:217]
	s_setprio 0
	s_setprio 1
	v_mfma_f32_16x16x128_f8f6f4 v[114:117], v[138:145], v[18:25], v[114:117]
	v_mfma_f32_16x16x128_f8f6f4 v[106:109], v[146:153], v[18:25], v[106:109]
	v_mfma_f32_16x16x128_f8f6f4 v[98:101], v[138:145], v[26:33], v[98:101]
	v_mfma_f32_16x16x128_f8f6f4 v[90:93], v[146:153], v[26:33], v[170:173]
	v_mfma_f32_16x16x128_f8f6f4 v[82:85], v[138:145], v[34:41], v[174:177]
	v_mfma_f32_16x16x128_f8f6f4 v[74:77], v[146:153], v[34:41], v[186:189]
	v_mfma_f32_16x16x128_f8f6f4 v[70:73], v[138:145], v[42:49], v[190:193]
	v_mfma_f32_16x16x128_f8f6f4 v[66:69], v[146:153], v[42:49], v[194:197]
	s_setprio 0
	s_barrier
	v_mov_b32_e32 v0, v132
	ds_read_b128 v[154:157], v137 offset:49152
	ds_read_b128 v[158:161], v137 offset:50176
	ds_read_b128 v[162:165], v137 offset:51200
	ds_read_b128 v[166:169], v137 offset:52224
	ds_read_b128 v[170:173], v137 offset:53248
	ds_read_b128 v[174:177], v137 offset:54272
	ds_read_b128 v[186:189], v137 offset:55296
	ds_read_b128 v[190:193], v137 offset:56320
	s_mov_b32 m0, s44
	v_lshl_add_u64 v[18:19], s[24:25], 0, v[0:1]
	v_lshl_add_u64 v[18:19], v[18:19], 0, s[82:83]
	v_mov_b32_e32 v0, v134
	global_load_lds_dwordx4 v[18:19], off
	s_mov_b32 m0, s45
	v_lshl_add_u64 v[18:19], s[24:25], 0, v[0:1]
	v_lshl_add_u64 v[18:19], v[18:19], 0, s[82:83]
	s_add_u32 s24, s24, 0x20080
	v_mov_b32_e32 v0, v132
	global_load_lds_dwordx4 v[18:19], off
	s_addc_u32 s25, s25, 0
	s_mov_b32 m0, s49
	s_nop 0
	global_load_lds_dwordx4 v0, s[24:25]
	v_mov_b32_e32 v0, v134
	s_mov_b32 m0, s50
	s_nop 0
	global_load_lds_dwordx4 v0, s[24:25]
	v_mov_b32_e32 v0, v133
	s_mov_b32 m0, s46
	v_lshl_add_u64 v[18:19], s[22:23], 0, v[0:1]
	v_lshl_add_u64 v[18:19], v[18:19], 0, s[82:83]
	v_mov_b32_e32 v0, v135
	global_load_lds_dwordx4 v[18:19], off
	s_mov_b32 m0, s47
	v_lshl_add_u64 v[18:19], s[22:23], 0, v[0:1]
	v_lshl_add_u64 v[18:19], v[18:19], 0, s[82:83]
	global_load_lds_dwordx4 v[18:19], off
	s_waitcnt vmcnt(8)
	s_waitcnt lgkmcnt(0)
	s_barrier
	s_setprio 1
	s_waitcnt lgkmcnt(0)
	v_mfma_f32_16x16x128_f8f6f4 v[62:65], v[2:9], v[154:161], v[62:65]
	v_mfma_f32_16x16x128_f8f6f4 v[58:61], v[10:17], v[154:161], v[58:61]
	v_mfma_f32_16x16x128_f8f6f4 v[54:57], v[2:9], v[162:169], v[54:57]
	v_mfma_f32_16x16x128_f8f6f4 v[46:49], v[10:17], v[162:169], v[198:201]
	v_mfma_f32_16x16x128_f8f6f4 v[38:41], v[2:9], v[170:177], v[202:205]
	v_mfma_f32_16x16x128_f8f6f4 v[30:33], v[10:17], v[170:177], v[206:209]
	v_mfma_f32_16x16x128_f8f6f4 v[22:25], v[2:9], v[186:193], v[218:221]
	v_mfma_f32_16x16x128_f8f6f4 v[14:17], v[10:17], v[186:193], v[222:225]
	s_setprio 0
	s_setprio 1
	v_mfma_f32_16x16x128_f8f6f4 v[50:53], v[138:145], v[154:161], v[50:53]
	v_mfma_f32_16x16x128_f8f6f4 v[42:45], v[146:153], v[154:161], v[226:229]
	v_mfma_f32_16x16x128_f8f6f4 v[34:37], v[138:145], v[162:169], v[230:233]
	v_mfma_f32_16x16x128_f8f6f4 v[26:29], v[146:153], v[162:169], v[234:237]
	v_mfma_f32_16x16x128_f8f6f4 v[18:21], v[138:145], v[170:177], v[238:241]
	v_mfma_f32_16x16x128_f8f6f4 v[10:13], v[146:153], v[170:177], v[244:247]
	v_mfma_f32_16x16x128_f8f6f4 v[6:9], v[138:145], v[186:193], v[248:251]
	v_mfma_f32_16x16x128_f8f6f4 v[2:5], v[146:153], v[186:193], v[182:185]
	s_setprio 0
	s_barrier
	s_add_i32 s58, s58, 2
	s_add_u32 s56, s56, 0x100
	s_addc_u32 s57, s57, 0
	s_add_u32 s20, s20, 0x100
	s_addc_u32 s21, s21, 0
	s_cmp_gt_u32 s58, 5
	s_cbranch_scc0 .LBB0_578
	s_and_b64 vcc, exec, s[8:9]
	s_cbranch_vccz .LBB0_581
	s_barrier

.Llzf_4:
	v_mfma_f32_16x16x128_f8f6f4 v[126:129], v[130:137], v[186:193], 0
	v_mfma_f32_16x16x128_f8f6f4 v[122:125], v[138:145], v[186:193], 0
	v_mfma_f32_16x16x128_f8f6f4 v[110:113], v[130:137], v[194:201], 0
	v_mfma_f32_16x16x128_f8f6f4 v[106:109], v[138:145], v[194:201], 0
	v_mfma_f32_16x16x128_f8f6f4 v[98:101], v[130:137], v[202:209], 0
	v_mfma_f32_16x16x128_f8f6f4 v[162:165], v[138:145], v[202:209], 0
	v_mfma_f32_16x16x128_f8f6f4 v[172:175], v[130:137], v[210:217], 0
	v_mfma_f32_16x16x128_f8f6f4 v[176:179], v[138:145], v[210:217], 0
	s_setprio 0
	s_setprio 1
	v_mfma_f32_16x16x128_f8f6f4 v[118:121], v[146:153], v[186:193], 0
	v_mfma_f32_16x16x128_f8f6f4 v[114:117], v[154:161], v[186:193], 0
	v_mfma_f32_16x16x128_f8f6f4 v[102:105], v[146:153], v[194:201], 0
	v_mfma_f32_16x16x128_f8f6f4 v[180:183], v[154:161], v[194:201], 0
	v_mfma_f32_16x16x128_f8f6f4 v[184:187], v[146:153], v[202:209], 0
	v_mfma_f32_16x16x128_f8f6f4 v[188:191], v[154:161], v[202:209], 0
	v_mfma_f32_16x16x128_f8f6f4 v[192:195], v[146:153], v[210:217], 0
	v_mfma_f32_16x16x128_f8f6f4 v[196:199], v[154:161], v[210:217], 0
	s_branch .Llzj_4
.Llzg_4:
	v_mfma_f32_16x16x128_f8f6f4 v[62:65], v[130:137], v[66:73], 0
	v_mfma_f32_16x16x128_f8f6f4 v[58:61], v[138:145], v[66:73], 0
	v_mfma_f32_16x16x128_f8f6f4 v[50:53], v[130:137], v[74:81], 0
	v_mfma_f32_16x16x128_f8f6f4 v[202:205], v[138:145], v[74:81], 0
	v_mfma_f32_16x16x128_f8f6f4 v[206:209], v[130:137], v[82:89], 0
	v_mfma_f32_16x16x128_f8f6f4 v[210:213], v[138:145], v[82:89], 0
	v_mfma_f32_16x16x128_f8f6f4 v[214:217], v[130:137], v[90:97], 0
	v_mfma_f32_16x16x128_f8f6f4 v[218:221], v[138:145], v[90:97], 0
	s_setprio 0
	s_setprio 1
	v_mfma_f32_16x16x128_f8f6f4 v[54:57], v[146:153], v[66:73], 0
	v_mfma_f32_16x16x128_f8f6f4 v[222:225], v[154:161], v[66:73], 0
	v_mfma_f32_16x16x128_f8f6f4 v[226:229], v[146:153], v[74:81], 0
	v_mfma_f32_16x16x128_f8f6f4 v[230:233], v[154:161], v[74:81], 0
	v_mfma_f32_16x16x128_f8f6f4 v[234:237], v[146:153], v[82:89], 0
	v_mfma_f32_16x16x128_f8f6f4 v[238:241], v[154:161], v[82:89], 0
	v_mfma_f32_16x16x128_f8f6f4 v[244:247], v[146:153], v[90:97], 0
	v_mfma_f32_16x16x128_f8f6f4 v[248:251], v[154:161], v[90:97], 0
	s_branch .Llzk_4

.Llzj_4:
	s_setprio 0
	s_barrier
	v_mov_b32_e32 v0, v166
	s_mov_b32 m0, s37
	s_nop 2
	ds_read_b128 v[66:69], v171 offset:16384
	ds_read_b128 v[70:73], v171 offset:17408
	ds_read_b128 v[74:77], v171 offset:18432
	ds_read_b128 v[78:81], v171 offset:19456
	ds_read_b128 v[82:85], v171 offset:20480
	ds_read_b128 v[86:89], v171 offset:21504
	ds_read_b128 v[90:93], v171 offset:22528
	ds_read_b128 v[94:97], v171 offset:23552
	s_add_u32 s62, s26, 0x20000
	global_load_lds_dwordx4 v0, s[26:27]
	v_mov_b32_e32 v0, v168
	s_mov_b32 m0, s38
	s_addc_u32 s63, s27, 0
	global_load_lds_dwordx4 v0, s[26:27]
	v_mov_b32_e32 v0, v166
	s_mov_b32 m0, s40
	s_nop 0
	global_load_lds_dwordx4 v0, s[62:63]
	v_mov_b32_e32 v0, v168
	s_mov_b32 m0, s41
	s_nop 0
	global_load_lds_dwordx4 v0, s[62:63]
	v_mov_b32_e32 v0, v167
	s_mov_b32 m0, s42
	s_nop 0
	global_load_lds_dwordx4 v0, s[24:25]
	v_mov_b32_e32 v0, v169
	s_mov_b32 m0, s43
	s_nop 0
	global_load_lds_dwordx4 v0, s[24:25]
	s_waitcnt vmcnt(8)
	s_waitcnt lgkmcnt(0)
	s_barrier
	s_setprio 1
	s_waitcnt lgkmcnt(0)
	s_cmp_eq_u32 s61, -2
	s_cbranch_scc1 .Llzg_4
	v_mfma_f32_16x16x128_f8f6f4 v[62:65], v[130:137], v[66:73], v[62:65]
	v_mfma_f32_16x16x128_f8f6f4 v[58:61], v[138:145], v[66:73], v[58:61]
	v_mfma_f32_16x16x128_f8f6f4 v[50:53], v[130:137], v[74:81], v[50:53]
	v_mfma_f32_16x16x128_f8f6f4 v[202:205], v[138:145], v[74:81], v[42:45]
	v_mfma_f32_16x16x128_f8f6f4 v[206:209], v[130:137], v[82:89], v[34:37]
	v_mfma_f32_16x16x128_f8f6f4 v[210:213], v[138:145], v[82:89], v[26:29]
	v_mfma_f32_16x16x128_f8f6f4 v[214:217], v[130:137], v[90:97], v[18:21]
	v_mfma_f32_16x16x128_f8f6f4 v[218:221], v[138:145], v[90:97], v[10:13]
	s_setprio 0
	s_setprio 1
	v_mfma_f32_16x16x128_f8f6f4 v[54:57], v[146:153], v[66:73], v[54:57]
	v_mfma_f32_16x16x128_f8f6f4 v[222:225], v[154:161], v[66:73], v[46:49]
	v_mfma_f32_16x16x128_f8f6f4 v[226:229], v[146:153], v[74:81], v[38:41]
	v_mfma_f32_16x16x128_f8f6f4 v[230:233], v[154:161], v[74:81], v[30:33]
	v_mfma_f32_16x16x128_f8f6f4 v[234:237], v[146:153], v[82:89], v[22:25]
	v_mfma_f32_16x16x128_f8f6f4 v[238:241], v[154:161], v[82:89], v[14:17]
	v_mfma_f32_16x16x128_f8f6f4 v[244:247], v[146:153], v[90:97], v[6:9]
	v_mfma_f32_16x16x128_f8f6f4 v[248:251], v[154:161], v[90:97], v[2:5]
.Llzk_4:
	s_setprio 0
	s_barrier
	v_add_u32_e32 v0, s48, v170
	s_nop 3
	ds_read_b128 v[2:5], v0
	ds_read_b128 v[6:9], v0 offset:1024
	ds_read_b128 v[10:13], v0 offset:2048
	ds_read_b128 v[14:17], v0 offset:3072
	v_add_u32_e32 v0, s53, v170
	ds_read_b128 v[130:133], v0
	ds_read_b128 v[134:137], v0 offset:1024
	ds_read_b128 v[138:141], v0 offset:2048
	ds_read_b128 v[142:145], v0 offset:3072
	v_mov_b32_e32 v0, v167
	ds_read_b128 v[18:21], v171 offset:32768
	ds_read_b128 v[22:25], v171 offset:33792
	ds_read_b128 v[26:29], v171 offset:34816
	ds_read_b128 v[30:33], v171 offset:35840
	ds_read_b128 v[34:37], v171 offset:36864
	ds_read_b128 v[38:41], v171 offset:37888
	ds_read_b128 v[42:45], v171 offset:38912
	ds_read_b128 v[46:49], v171 offset:39936
	s_mov_b32 m0, s44
	v_add_u32_e32 v0, 0x20000, v0
	global_load_lds_dwordx4 v0, s[24:25]
	v_mov_b32_e32 v0, v169
	s_mov_b32 m0, s45
	v_add_u32_e32 v0, 0x20000, v0
	global_load_lds_dwordx4 v0, s[24:25]
	s_waitcnt vmcnt(8)
	s_waitcnt lgkmcnt(0)
	s_barrier
	s_setprio 1
	s_waitcnt lgkmcnt(0)
	v_mfma_f32_16x16x128_f8f6f4 v[126:129], v[2:9], v[18:25], v[126:129]
	v_mfma_f32_16x16x128_f8f6f4 v[122:125], v[10:17], v[18:25], v[122:125]
	v_mfma_f32_16x16x128_f8f6f4 v[110:113], v[2:9], v[26:33], v[110:113]
	v_mfma_f32_16x16x128_f8f6f4 v[106:109], v[10:17], v[26:33], v[106:109]
	v_mfma_f32_16x16x128_f8f6f4 v[98:101], v[2:9], v[34:41], v[98:101]
	v_mfma_f32_16x16x128_f8f6f4 v[90:93], v[10:17], v[34:41], v[162:165]
	v_mfma_f32_16x16x128_f8f6f4 v[82:85], v[2:9], v[42:49], v[172:175]
	v_mfma_f32_16x16x128_f8f6f4 v[74:77], v[10:17], v[42:49], v[176:179]
	s_setprio 0
	s_setprio 1
	v_mfma_f32_16x16x128_f8f6f4 v[118:121], v[130:137], v[18:25], v[118:121]
	v_mfma_f32_16x16x128_f8f6f4 v[114:117], v[138:145], v[18:25], v[114:117]
	v_mfma_f32_16x16x128_f8f6f4 v[102:105], v[130:137], v[26:33], v[102:105]
	v_mfma_f32_16x16x128_f8f6f4 v[94:97], v[138:145], v[26:33], v[180:183]
	v_mfma_f32_16x16x128_f8f6f4 v[86:89], v[130:137], v[34:41], v[184:187]
	v_mfma_f32_16x16x128_f8f6f4 v[78:81], v[138:145], v[34:41], v[188:191]
	v_mfma_f32_16x16x128_f8f6f4 v[70:73], v[130:137], v[42:49], v[192:195]
	v_mfma_f32_16x16x128_f8f6f4 v[66:69], v[138:145], v[42:49], v[196:199]
	s_setprio 0
	s_barrier
	v_mov_b32_e32 v0, v166
	ds_read_b128 v[146:149], v171 offset:49152
	ds_read_b128 v[150:153], v171 offset:50176
	ds_read_b128 v[154:157], v171 offset:51200
	ds_read_b128 v[158:161], v171 offset:52224
	ds_read_b128 v[186:189], v171 offset:53248
	ds_read_b128 v[190:193], v171 offset:54272
	ds_read_b128 v[194:197], v171 offset:55296
	ds_read_b128 v[198:201], v171 offset:56320
	s_mov_b32 m0, s49
	v_lshl_add_u64 v[18:19], s[26:27], 0, v[0:1]
	v_lshl_add_u64 v[18:19], v[18:19], 0, s[82:83]
	v_mov_b32_e32 v0, v168
	global_load_lds_dwordx4 v[18:19], off
	s_mov_b32 m0, s50
	v_lshl_add_u64 v[18:19], s[26:27], 0, v[0:1]
	v_lshl_add_u64 v[18:19], v[18:19], 0, s[82:83]
	s_add_u32 s26, s26, 0x20080
	v_mov_b32_e32 v0, v166
	global_load_lds_dwordx4 v[18:19], off
	s_addc_u32 s27, s27, 0
	s_mov_b32 m0, s54
	s_nop 0
	global_load_lds_dwordx4 v0, s[26:27]
	v_mov_b32_e32 v0, v168
	s_mov_b32 m0, s55
	s_nop 0
	global_load_lds_dwordx4 v0, s[26:27]
	v_mov_b32_e32 v0, v167
	s_mov_b32 m0, s51
	v_lshl_add_u64 v[18:19], s[24:25], 0, v[0:1]
	v_lshl_add_u64 v[18:19], v[18:19], 0, s[82:83]
	v_mov_b32_e32 v0, v169
	global_load_lds_dwordx4 v[18:19], off
	s_mov_b32 m0, s52
	v_lshl_add_u64 v[18:19], s[24:25], 0, v[0:1]
	v_lshl_add_u64 v[18:19], v[18:19], 0, s[82:83]
	global_load_lds_dwordx4 v[18:19], off
	s_waitcnt vmcnt(8)
	s_waitcnt lgkmcnt(0)
	s_barrier
	s_setprio 1
	s_waitcnt lgkmcnt(0)
	v_mfma_f32_16x16x128_f8f6f4 v[62:65], v[2:9], v[146:153], v[62:65]
	v_mfma_f32_16x16x128_f8f6f4 v[58:61], v[10:17], v[146:153], v[58:61]
	v_mfma_f32_16x16x128_f8f6f4 v[50:53], v[2:9], v[154:161], v[50:53]
	v_mfma_f32_16x16x128_f8f6f4 v[42:45], v[10:17], v[154:161], v[202:205]
	v_mfma_f32_16x16x128_f8f6f4 v[34:37], v[2:9], v[186:193], v[206:209]
	v_mfma_f32_16x16x128_f8f6f4 v[26:29], v[10:17], v[186:193], v[210:213]
	v_mfma_f32_16x16x128_f8f6f4 v[18:21], v[2:9], v[194:201], v[214:217]
	v_mfma_f32_16x16x128_f8f6f4 v[10:13], v[10:17], v[194:201], v[218:221]
	s_setprio 0
	s_setprio 1
	v_mfma_f32_16x16x128_f8f6f4 v[54:57], v[130:137], v[146:153], v[54:57]
	v_mfma_f32_16x16x128_f8f6f4 v[46:49], v[138:145], v[146:153], v[222:225]
	v_mfma_f32_16x16x128_f8f6f4 v[38:41], v[130:137], v[154:161], v[226:229]
	v_mfma_f32_16x16x128_f8f6f4 v[30:33], v[138:145], v[154:161], v[230:233]
	v_mfma_f32_16x16x128_f8f6f4 v[22:25], v[130:137], v[186:193], v[234:237]
	v_mfma_f32_16x16x128_f8f6f4 v[14:17], v[138:145], v[186:193], v[238:241]
	v_mfma_f32_16x16x128_f8f6f4 v[6:9], v[130:137], v[194:201], v[244:247]
	v_mfma_f32_16x16x128_f8f6f4 v[2:5], v[138:145], v[194:201], v[248:251]
	s_setprio 0
	s_barrier
	s_add_i32 s61, s61, 2
	s_add_u32 s59, s59, 0x100
	s_addc_u32 s60, s60, 0
	s_add_u32 s22, s22, 0x100
	s_addc_u32 s23, s23, 0
	s_cmp_gt_u32 s61, 5
	s_cbranch_scc0 .LBB0_595
	s_and_b64 vcc, exec, s[10:11]
	s_cbranch_vccz .LBB0_598
	s_barrier

.Llzf_1:
	v_mfma_f32_16x16x128_f8f6f4 v[142:145], v[154:161], v[194:201], 0
	v_mfma_f32_16x16x128_f8f6f4 v[134:137], v[162:169], v[194:201], 0
	v_mfma_f32_16x16x128_f8f6f4 v[126:129], v[154:161], v[202:209], 0
	v_mfma_f32_16x16x128_f8f6f4 v[118:121], v[162:169], v[202:209], 0
	v_mfma_f32_16x16x128_f8f6f4 v[110:113], v[154:161], v[210:217], 0
	v_mfma_f32_16x16x128_f8f6f4 v[102:105], v[162:169], v[210:217], 0
	v_mfma_f32_16x16x128_f8f6f4 v[178:181], v[154:161], v[244:251], 0
	v_mfma_f32_16x16x128_f8f6f4 v[182:185], v[162:169], v[244:251], 0
	s_setprio 0
	s_setprio 1
	v_mfma_f32_16x16x128_f8f6f4 v[138:141], v[170:177], v[194:201], 0
	v_mfma_f32_16x16x128_f8f6f4 v[130:133], v[186:193], v[194:201], 0
	v_mfma_f32_16x16x128_f8f6f4 v[122:125], v[170:177], v[202:209], 0
	v_mfma_f32_16x16x128_f8f6f4 v[114:117], v[186:193], v[202:209], 0
	v_mfma_f32_16x16x128_f8f6f4 v[106:109], v[170:177], v[210:217], 0
	v_mfma_f32_16x16x128_f8f6f4 v[194:197], v[186:193], v[210:217], 0
	v_mfma_f32_16x16x128_f8f6f4 v[198:201], v[170:177], v[244:251], 0
	v_mfma_f32_16x16x128_f8f6f4 v[202:205], v[186:193], v[244:251], 0
	s_branch .Llzj_1
.Llzg_1:
	v_mfma_f32_16x16x128_f8f6f4 v[62:65], v[154:161], v[68:75], 0
	v_mfma_f32_16x16x128_f8f6f4 v[54:57], v[162:169], v[68:75], 0
	s_waitcnt lgkmcnt(0)
	v_mfma_f32_16x16x128_f8f6f4 v[46:49], v[154:161], v[76:83], 0
	v_mfma_f32_16x16x128_f8f6f4 v[218:221], v[162:169], v[76:83], 0
	v_mfma_f32_16x16x128_f8f6f4 v[222:225], v[154:161], v[84:91], 0
	v_mfma_f32_16x16x128_f8f6f4 v[226:229], v[162:169], v[84:91], 0
	v_mfma_f32_16x16x128_f8f6f4 v[230:233], v[154:161], v[92:99], 0
	v_mfma_f32_16x16x128_f8f6f4 v[234:237], v[162:169], v[92:99], 0
	s_setprio 0
	s_setprio 1
	v_mfma_f32_16x16x128_f8f6f4 v[58:61], v[170:177], v[68:75], 0
	v_mfma_f32_16x16x128_f8f6f4 v[50:53], v[186:193], v[68:75], 0
	v_mfma_f32_16x16x128_f8f6f4 v[42:45], v[170:177], v[76:83], 0
	v_mfma_f32_16x16x128_f8f6f4 v[74:77], v[186:193], v[76:83], 0
	v_mfma_f32_16x16x128_f8f6f4 v[238:241], v[170:177], v[84:91], 0
	v_mfma_f32_16x16x128_f8f6f4 v[82:85], v[186:193], v[84:91], 0
	v_mfma_f32_16x16x128_f8f6f4 v[244:247], v[170:177], v[92:99], 0
	v_mfma_f32_16x16x128_f8f6f4 v[90:93], v[186:193], v[92:99], 0
	s_branch .Llzk_1

.Llzj_1:
	s_setprio 0
	s_barrier
	v_lshl_add_u32 v0, s36, 10, v150
	ds_read2st64_b32 v[76:77], v0 offset1:1
	s_nop 2
	ds_read_b128 v[68:71], v153 offset:16384
	ds_read_b128 v[72:75], v153 offset:17408
	v_mov_b32_e32 v101, v148
	s_mov_b32 m0, s41
	s_waitcnt lgkmcnt(0)
	v_lshl_add_u32 v67, v76, 10, v151
	v_lshl_add_u32 v100, v77, 10, v151
	ds_read_b128 v[76:79], v153 offset:18432
	ds_read_b128 v[80:83], v153 offset:19456
	ds_read_b128 v[84:87], v153 offset:20480
	ds_read_b128 v[88:91], v153 offset:21504
	ds_read_b128 v[92:95], v153 offset:22528
	ds_read_b128 v[96:99], v153 offset:23552
	s_add_u32 s36, s30, 0x20000
	global_load_lds_dwordx4 v101, s[30:31]
	v_mov_b32_e32 v101, v149
	s_mov_b32 m0, s42
	s_addc_u32 s37, s31, 0
	global_load_lds_dwordx4 v101, s[30:31]
	v_mov_b32_e32 v101, v148
	s_mov_b32 m0, s44
	s_nop 0
	global_load_lds_dwordx4 v101, s[36:37]
	v_mov_b32_e32 v101, v149
	s_mov_b32 m0, s45
	s_nop 0
	global_load_lds_dwordx4 v101, s[36:37]
	s_mov_b32 m0, s46
	s_nop 0
	global_load_lds_dwordx4 v67, s[34:35]
	s_mov_b32 m0, s47
	s_nop 0
	global_load_lds_dwordx4 v100, s[34:35]
	s_waitcnt vmcnt(8)
	s_waitcnt lgkmcnt(0)
	s_barrier
	s_setprio 1
	s_cmp_eq_u32 s67, -2
	s_cbranch_scc1 .Llzg_1
	v_mfma_f32_16x16x128_f8f6f4 v[62:65], v[154:161], v[68:75], v[62:65]
	v_mfma_f32_16x16x128_f8f6f4 v[54:57], v[162:169], v[68:75], v[54:57]
	s_waitcnt lgkmcnt(0)
	v_mfma_f32_16x16x128_f8f6f4 v[46:49], v[154:161], v[76:83], v[46:49]
	v_mfma_f32_16x16x128_f8f6f4 v[218:221], v[162:169], v[76:83], v[38:41]
	v_mfma_f32_16x16x128_f8f6f4 v[222:225], v[154:161], v[84:91], v[30:33]
	v_mfma_f32_16x16x128_f8f6f4 v[226:229], v[162:169], v[84:91], v[22:25]
	v_mfma_f32_16x16x128_f8f6f4 v[230:233], v[154:161], v[92:99], v[14:17]
	v_mfma_f32_16x16x128_f8f6f4 v[234:237], v[162:169], v[92:99], v[6:9]
	s_setprio 0
	s_setprio 1
	v_mfma_f32_16x16x128_f8f6f4 v[58:61], v[170:177], v[68:75], v[58:61]
	v_mfma_f32_16x16x128_f8f6f4 v[50:53], v[186:193], v[68:75], v[50:53]
	v_mfma_f32_16x16x128_f8f6f4 v[42:45], v[170:177], v[76:83], v[42:45]
	v_mfma_f32_16x16x128_f8f6f4 v[74:77], v[186:193], v[76:83], v[34:37]
	v_mfma_f32_16x16x128_f8f6f4 v[238:241], v[170:177], v[84:91], v[26:29]
	v_mfma_f32_16x16x128_f8f6f4 v[82:85], v[186:193], v[84:91], v[18:21]
	v_mfma_f32_16x16x128_f8f6f4 v[244:247], v[170:177], v[92:99], v[10:13]
	v_mfma_f32_16x16x128_f8f6f4 v[90:93], v[186:193], v[92:99], v[2:5]
.Llzk_1:
	s_setprio 0
	s_barrier
	s_nop 4
	ds_read2st64_b32 v[2:3], v0 offset0:2 offset1:3
	v_add_u32_e32 v10, s52, v152
	s_waitcnt lgkmcnt(0)
	v_lshl_add_u32 v67, v2, 10, v151
	v_lshl_add_u32 v68, v3, 10, v151
	ds_read_b128 v[2:5], v10
	ds_read_b128 v[6:9], v10 offset:1024
	ds_read_b128 v[154:157], v10 offset:2048
	ds_read_b128 v[158:161], v10 offset:3072
	v_add_u32_e32 v10, s57, v152
	ds_read_b128 v[162:165], v10
	ds_read_b128 v[166:169], v10 offset:1024
	ds_read_b128 v[170:173], v10 offset:2048
	ds_read_b128 v[174:177], v10 offset:3072
	s_mov_b32 m0, s48
	ds_read_b128 v[10:13], v153 offset:32768
	ds_read_b128 v[14:17], v153 offset:33792
	ds_read_b128 v[18:21], v153 offset:34816
	ds_read_b128 v[22:25], v153 offset:35840
	ds_read_b128 v[26:29], v153 offset:36864
	ds_read_b128 v[30:33], v153 offset:37888
	ds_read_b128 v[34:37], v153 offset:38912
	ds_read_b128 v[38:41], v153 offset:39936
	s_nop 0
	global_load_lds_dwordx4 v67, s[34:35]
	s_mov_b32 m0, s49
	s_nop 0
	global_load_lds_dwordx4 v68, s[34:35]
	s_waitcnt vmcnt(8)
	s_waitcnt lgkmcnt(0)
	s_barrier
	s_setprio 1
	s_waitcnt lgkmcnt(0)
	v_mfma_f32_16x16x128_f8f6f4 v[142:145], v[2:9], v[10:17], v[142:145]
	v_mfma_f32_16x16x128_f8f6f4 v[134:137], v[154:161], v[10:17], v[134:137]
	v_mfma_f32_16x16x128_f8f6f4 v[126:129], v[2:9], v[18:25], v[126:129]
	v_mfma_f32_16x16x128_f8f6f4 v[118:121], v[154:161], v[18:25], v[118:121]
	v_mfma_f32_16x16x128_f8f6f4 v[110:113], v[2:9], v[26:33], v[110:113]
	v_mfma_f32_16x16x128_f8f6f4 v[102:105], v[154:161], v[26:33], v[102:105]
	v_mfma_f32_16x16x128_f8f6f4 v[94:97], v[2:9], v[34:41], v[178:181]
	v_mfma_f32_16x16x128_f8f6f4 v[78:81], v[154:161], v[34:41], v[182:185]
	s_setprio 0
	s_setprio 1
	v_mfma_f32_16x16x128_f8f6f4 v[138:141], v[162:169], v[10:17], v[138:141]
	v_mfma_f32_16x16x128_f8f6f4 v[130:133], v[170:177], v[10:17], v[130:133]
	v_mfma_f32_16x16x128_f8f6f4 v[122:125], v[162:169], v[18:25], v[122:125]
	v_mfma_f32_16x16x128_f8f6f4 v[114:117], v[170:177], v[18:25], v[114:117]
	v_mfma_f32_16x16x128_f8f6f4 v[106:109], v[162:169], v[26:33], v[106:109]
	v_mfma_f32_16x16x128_f8f6f4 v[98:101], v[170:177], v[26:33], v[194:197]
	v_mfma_f32_16x16x128_f8f6f4 v[86:89], v[162:169], v[34:41], v[198:201]
	v_mfma_f32_16x16x128_f8f6f4 v[70:73], v[170:177], v[34:41], v[202:205]
	s_setprio 0
	s_barrier
	ds_read2st64_b32 v[10:11], v0 offset1:1
	ds_read_b128 v[186:189], v153 offset:49152
	ds_read_b128 v[190:193], v153 offset:50176
	v_mov_b32_e32 v0, v148
	ds_read_b128 v[194:197], v153 offset:51200
	ds_read_b128 v[198:201], v153 offset:52224
	ds_read_b128 v[202:205], v153 offset:53248
	ds_read_b128 v[206:209], v153 offset:54272
	ds_read_b128 v[210:213], v153 offset:55296
	ds_read_b128 v[214:217], v153 offset:56320
	s_mov_b32 m0, s53
	v_lshl_add_u64 v[14:15], s[30:31], 0, v[0:1]
	v_lshl_add_u64 v[14:15], v[14:15], 0, s[82:83]
	v_mov_b32_e32 v0, v149
	global_load_lds_dwordx4 v[14:15], off
	s_mov_b32 m0, s54
	v_lshl_add_u64 v[14:15], s[30:31], 0, v[0:1]
	v_lshl_add_u64 v[14:15], v[14:15], 0, s[82:83]
	s_add_u32 s30, s30, 0x20080
	v_mov_b32_e32 v0, v148
	global_load_lds_dwordx4 v[14:15], off
	s_addc_u32 s31, s31, 0
	s_mov_b32 m0, s58
	s_waitcnt lgkmcnt(0)
	v_lshl_add_u32 v10, v10, 10, v151
	global_load_lds_dwordx4 v0, s[30:31]
	v_mov_b32_e32 v0, v149
	s_mov_b32 m0, s59
	v_lshl_add_u32 v12, v11, 10, v151
	v_mov_b32_e32 v11, v1
	global_load_lds_dwordx4 v0, s[30:31]
	s_mov_b32 m0, s55
	v_lshl_add_u64 v[10:11], s[34:35], 0, v[10:11]
	v_lshl_add_u64 v[10:11], v[10:11], 0, s[82:83]
	v_mov_b32_e32 v13, v1
	global_load_lds_dwordx4 v[10:11], off
	s_mov_b32 m0, s56
	v_lshl_add_u64 v[10:11], s[34:35], 0, v[12:13]
	v_lshl_add_u64 v[10:11], v[10:11], 0, s[82:83]
	global_load_lds_dwordx4 v[10:11], off
	s_waitcnt vmcnt(8)
	s_waitcnt lgkmcnt(0)
	s_barrier
	s_setprio 1
	v_mfma_f32_16x16x128_f8f6f4 v[62:65], v[2:9], v[186:193], v[62:65]
	v_mfma_f32_16x16x128_f8f6f4 v[54:57], v[154:161], v[186:193], v[54:57]
	v_mfma_f32_16x16x128_f8f6f4 v[46:49], v[2:9], v[194:201], v[46:49]
	v_mfma_f32_16x16x128_f8f6f4 v[38:41], v[154:161], v[194:201], v[218:221]
	v_mfma_f32_16x16x128_f8f6f4 v[30:33], v[2:9], v[202:209], v[222:225]
	v_mfma_f32_16x16x128_f8f6f4 v[22:25], v[154:161], v[202:209], v[226:229]
	v_mfma_f32_16x16x128_f8f6f4 v[14:17], v[2:9], v[210:217], v[230:233]
	v_mfma_f32_16x16x128_f8f6f4 v[6:9], v[154:161], v[210:217], v[234:237]
	s_setprio 0
	s_setprio 1
	v_mfma_f32_16x16x128_f8f6f4 v[58:61], v[162:169], v[186:193], v[58:61]
	v_mfma_f32_16x16x128_f8f6f4 v[50:53], v[170:177], v[186:193], v[50:53]
	v_mfma_f32_16x16x128_f8f6f4 v[42:45], v[162:169], v[194:201], v[42:45]
	v_mfma_f32_16x16x128_f8f6f4 v[34:37], v[170:177], v[194:201], v[74:77]
	v_mfma_f32_16x16x128_f8f6f4 v[26:29], v[162:169], v[202:209], v[238:241]
	v_mfma_f32_16x16x128_f8f6f4 v[18:21], v[170:177], v[202:209], v[82:85]
	v_mfma_f32_16x16x128_f8f6f4 v[10:13], v[162:169], v[210:217], v[244:247]
	v_mfma_f32_16x16x128_f8f6f4 v[2:5], v[170:177], v[210:217], v[90:93]
	s_setprio 0
	s_barrier
	s_add_i32 s67, s67, 2
	s_add_u32 s65, s65, 0x100
	s_addc_u32 s66, s66, 0
	s_add_u32 s28, s28, 0x100
	s_addc_u32 s29, s29, 0
	s_cmp_gt_u32 s67, 5
	s_cbranch_scc0 .LBB0_1243
	s_and_b64 vcc, exec, s[16:17]
	s_cbranch_vccz .LBB0_1246
	s_barrier

.Llzf_0:
	v_mfma_f32_16x16x128_f8f6f4 v[126:129], v[132:139], v[186:193], 0
	v_mfma_f32_16x16x128_f8f6f4 v[122:125], v[140:147], v[186:193], 0
	v_mfma_f32_16x16x128_f8f6f4 v[118:121], v[132:139], v[194:201], 0
	v_mfma_f32_16x16x128_f8f6f4 v[114:117], v[140:147], v[194:201], 0
	v_mfma_f32_16x16x128_f8f6f4 v[110:113], v[132:139], v[202:209], 0
	v_mfma_f32_16x16x128_f8f6f4 v[106:109], v[140:147], v[202:209], 0
	v_mfma_f32_16x16x128_f8f6f4 v[172:175], v[132:139], v[210:217], 0
	v_mfma_f32_16x16x128_f8f6f4 v[176:179], v[140:147], v[210:217], 0
	s_setprio 0
	s_setprio 1
	v_mfma_f32_16x16x128_f8f6f4 v[70:73], v[148:155], v[186:193], 0
	v_mfma_f32_16x16x128_f8f6f4 v[62:65], v[156:163], v[186:193], 0
	v_mfma_f32_16x16x128_f8f6f4 v[180:183], v[148:155], v[194:201], 0
	v_mfma_f32_16x16x128_f8f6f4 v[184:187], v[156:163], v[194:201], 0
	v_mfma_f32_16x16x128_f8f6f4 v[188:191], v[148:155], v[202:209], 0
	v_mfma_f32_16x16x128_f8f6f4 v[192:195], v[156:163], v[202:209], 0
	v_mfma_f32_16x16x128_f8f6f4 v[196:199], v[148:155], v[210:217], 0
	v_mfma_f32_16x16x128_f8f6f4 v[200:203], v[156:163], v[210:217], 0
	s_branch .Llzj_0
.Llzg_0:
	v_mfma_f32_16x16x128_f8f6f4 v[94:97], v[132:139], v[34:41], 0
	v_mfma_f32_16x16x128_f8f6f4 v[90:93], v[140:147], v[34:41], 0
	v_mfma_f32_16x16x128_f8f6f4 v[86:89], v[132:139], v[42:49], 0
	v_mfma_f32_16x16x128_f8f6f4 v[82:85], v[140:147], v[42:49], 0
	v_mfma_f32_16x16x128_f8f6f4 v[66:69], v[132:139], v[98:105], 0
	v_mfma_f32_16x16x128_f8f6f4 v[58:61], v[140:147], v[98:105], 0
	v_mfma_f32_16x16x128_f8f6f4 v[204:207], v[132:139], v[50:57], 0
	v_mfma_f32_16x16x128_f8f6f4 v[208:211], v[140:147], v[50:57], 0
	s_setprio 0
	s_setprio 1
	v_mfma_f32_16x16x128_f8f6f4 v[212:215], v[148:155], v[34:41], 0
	v_mfma_f32_16x16x128_f8f6f4 v[216:219], v[156:163], v[34:41], 0
	v_mfma_f32_16x16x128_f8f6f4 v[220:223], v[148:155], v[42:49], 0
	v_mfma_f32_16x16x128_f8f6f4 v[224:227], v[156:163], v[42:49], 0
	v_mfma_f32_16x16x128_f8f6f4 v[228:231], v[148:155], v[50:57], 0
	v_mfma_f32_16x16x128_f8f6f4 v[232:235], v[156:163], v[50:57], 0
	v_mfma_f32_16x16x128_f8f6f4 v[236:239], v[148:155], v[98:105], 0
	v_mfma_f32_16x16x128_f8f6f4 v[244:247], v[156:163], v[98:105], 0
	s_branch .Llzk_0

.Llzj_0:
	s_setprio 0
	s_barrier
	v_mov_b32_e32 v0, v166
	s_mov_b32 m0, s25
	s_nop 2
	ds_read_b128 v[34:37], v171 offset:16384
	ds_read_b128 v[38:41], v171 offset:17408
	ds_read_b128 v[42:45], v171 offset:18432
	ds_read_b128 v[46:49], v171 offset:19456
	ds_read_b128 v[50:53], v171 offset:20480
	ds_read_b128 v[54:57], v171 offset:21504
	ds_read_b128 v[98:101], v171 offset:22528
	ds_read_b128 v[102:105], v171 offset:23552
	s_add_u32 s68, s30, 0x20000
	global_load_lds_dwordx4 v0, s[30:31]
	v_mov_b32_e32 v0, v168
	s_mov_b32 m0, s44
	s_addc_u32 s69, s31, 0
	global_load_lds_dwordx4 v0, s[30:31]
	v_mov_b32_e32 v0, v166
	s_mov_b32 m0, s46
	s_nop 0
	global_load_lds_dwordx4 v0, s[68:69]
	v_mov_b32_e32 v0, v168
	s_mov_b32 m0, s47
	s_nop 0
	global_load_lds_dwordx4 v0, s[68:69]
	v_mov_b32_e32 v0, v167
	s_mov_b32 m0, s48
	s_nop 0
	global_load_lds_dwordx4 v0, s[28:29]
	v_mov_b32_e32 v0, v169
	s_mov_b32 m0, s49
	s_nop 0
	global_load_lds_dwordx4 v0, s[28:29]
	s_waitcnt vmcnt(8)
	s_waitcnt lgkmcnt(0)
	s_barrier
	s_setprio 1
	s_waitcnt lgkmcnt(0)
	s_cmp_eq_u32 s67, -2
	s_cbranch_scc1 .Llzg_0
	v_mfma_f32_16x16x128_f8f6f4 v[94:97], v[132:139], v[34:41], v[94:97]
	v_mfma_f32_16x16x128_f8f6f4 v[90:93], v[140:147], v[34:41], v[90:93]
	v_mfma_f32_16x16x128_f8f6f4 v[86:89], v[132:139], v[42:49], v[86:89]
	v_mfma_f32_16x16x128_f8f6f4 v[82:85], v[140:147], v[42:49], v[82:85]
	v_mfma_f32_16x16x128_f8f6f4 v[66:69], v[132:139], v[98:105], v[66:69]
	v_mfma_f32_16x16x128_f8f6f4 v[58:61], v[140:147], v[98:105], v[58:61]
	v_mfma_f32_16x16x128_f8f6f4 v[204:207], v[132:139], v[50:57], v[78:81]
	v_mfma_f32_16x16x128_f8f6f4 v[208:211], v[140:147], v[50:57], v[74:77]
	s_setprio 0
	s_setprio 1
	v_mfma_f32_16x16x128_f8f6f4 v[212:215], v[148:155], v[34:41], v[30:33]
	v_mfma_f32_16x16x128_f8f6f4 v[216:219], v[156:163], v[34:41], v[26:29]
	v_mfma_f32_16x16x128_f8f6f4 v[220:223], v[148:155], v[42:49], v[22:25]
	v_mfma_f32_16x16x128_f8f6f4 v[224:227], v[156:163], v[42:49], v[18:21]
	v_mfma_f32_16x16x128_f8f6f4 v[228:231], v[148:155], v[50:57], v[14:17]
	v_mfma_f32_16x16x128_f8f6f4 v[232:235], v[156:163], v[50:57], v[10:13]
	v_mfma_f32_16x16x128_f8f6f4 v[236:239], v[148:155], v[98:105], v[6:9]
	v_mfma_f32_16x16x128_f8f6f4 v[244:247], v[156:163], v[98:105], v[2:5]
.Llzk_0:
	s_setprio 0
	s_barrier
	v_add_u32_e32 v0, s54, v170
	s_nop 3
	ds_read_b128 v[2:5], v0
	ds_read_b128 v[6:9], v0 offset:1024
	ds_read_b128 v[10:13], v0 offset:2048
	ds_read_b128 v[14:17], v0 offset:3072
	v_add_u32_e32 v0, s59, v170
	ds_read_b128 v[132:135], v0
	ds_read_b128 v[136:139], v0 offset:1024
	ds_read_b128 v[140:143], v0 offset:2048
	ds_read_b128 v[144:147], v0 offset:3072
	v_mov_b32_e32 v0, v167
	ds_read_b128 v[18:21], v171 offset:32768
	ds_read_b128 v[22:25], v171 offset:33792
	ds_read_b128 v[26:29], v171 offset:34816
	ds_read_b128 v[30:33], v171 offset:35840
	ds_read_b128 v[34:37], v171 offset:36864
	ds_read_b128 v[38:41], v171 offset:37888
	ds_read_b128 v[74:77], v171 offset:38912
	ds_read_b128 v[78:81], v171 offset:39936
	s_mov_b32 m0, s50
	v_add_u32_e32 v0, 0x20000, v0
	global_load_lds_dwordx4 v0, s[28:29]
	v_mov_b32_e32 v0, v169
	s_mov_b32 m0, s51
	v_add_u32_e32 v0, 0x20000, v0
	global_load_lds_dwordx4 v0, s[28:29]
	s_waitcnt vmcnt(8)
	s_waitcnt lgkmcnt(0)
	s_barrier
	s_setprio 1
	s_waitcnt lgkmcnt(0)
	v_mfma_f32_16x16x128_f8f6f4 v[126:129], v[2:9], v[18:25], v[126:129]
	v_mfma_f32_16x16x128_f8f6f4 v[122:125], v[10:17], v[18:25], v[122:125]
	v_mfma_f32_16x16x128_f8f6f4 v[118:121], v[2:9], v[26:33], v[118:121]
	v_mfma_f32_16x16x128_f8f6f4 v[114:117], v[10:17], v[26:33], v[114:117]
	v_mfma_f32_16x16x128_f8f6f4 v[110:113], v[2:9], v[34:41], v[110:113]
	v_mfma_f32_16x16x128_f8f6f4 v[106:109], v[10:17], v[34:41], v[106:109]
	v_mfma_f32_16x16x128_f8f6f4 v[102:105], v[2:9], v[74:81], v[172:175]
	v_mfma_f32_16x16x128_f8f6f4 v[98:101], v[10:17], v[74:81], v[176:179]
	s_setprio 0
	s_setprio 1
	v_mfma_f32_16x16x128_f8f6f4 v[70:73], v[132:139], v[18:25], v[70:73]
	v_mfma_f32_16x16x128_f8f6f4 v[62:65], v[140:147], v[18:25], v[62:65]
	v_mfma_f32_16x16x128_f8f6f4 v[54:57], v[132:139], v[26:33], v[180:183]
	v_mfma_f32_16x16x128_f8f6f4 v[50:53], v[140:147], v[26:33], v[184:187]
	v_mfma_f32_16x16x128_f8f6f4 v[46:49], v[132:139], v[34:41], v[188:191]
	v_mfma_f32_16x16x128_f8f6f4 v[42:45], v[140:147], v[34:41], v[192:195]
	v_mfma_f32_16x16x128_f8f6f4 v[38:41], v[132:139], v[74:81], v[196:199]
	v_mfma_f32_16x16x128_f8f6f4 v[34:37], v[140:147], v[74:81], v[200:203]
	s_setprio 0
	s_barrier
	v_mov_b32_e32 v0, v166
	ds_read_b128 v[18:21], v171 offset:49152
	ds_read_b128 v[22:25], v171 offset:50176
	ds_read_b128 v[148:151], v171 offset:51200
	ds_read_b128 v[152:155], v171 offset:52224
	ds_read_b128 v[156:159], v171 offset:53248
	ds_read_b128 v[160:163], v171 offset:54272
	ds_read_b128 v[186:189], v171 offset:55296
	ds_read_b128 v[190:193], v171 offset:56320
	s_mov_b32 m0, s55
	v_lshl_add_u64 v[26:27], s[30:31], 0, v[0:1]
	v_lshl_add_u64 v[26:27], v[26:27], 0, s[82:83]
	v_mov_b32_e32 v0, v168
	global_load_lds_dwordx4 v[26:27], off
	s_mov_b32 m0, s56
	v_lshl_add_u64 v[26:27], s[30:31], 0, v[0:1]
	v_lshl_add_u64 v[26:27], v[26:27], 0, s[82:83]
	s_add_u32 s30, s30, 0x20080
	v_mov_b32_e32 v0, v166
	global_load_lds_dwordx4 v[26:27], off
	s_addc_u32 s31, s31, 0
	s_mov_b32 m0, s60
	s_nop 0
	global_load_lds_dwordx4 v0, s[30:31]
	v_mov_b32_e32 v0, v168
	s_mov_b32 m0, s61
	s_nop 0
	global_load_lds_dwordx4 v0, s[30:31]
	v_mov_b32_e32 v0, v167
	s_mov_b32 m0, s57
	v_lshl_add_u64 v[26:27], s[28:29], 0, v[0:1]
	v_lshl_add_u64 v[26:27], v[26:27], 0, s[82:83]
	v_mov_b32_e32 v0, v169
	global_load_lds_dwordx4 v[26:27], off
	s_mov_b32 m0, s58
	v_lshl_add_u64 v[26:27], s[28:29], 0, v[0:1]
	v_lshl_add_u64 v[26:27], v[26:27], 0, s[82:83]
	global_load_lds_dwordx4 v[26:27], off
	s_waitcnt vmcnt(8)
	s_waitcnt lgkmcnt(0)
	s_barrier
	s_setprio 1
	s_waitcnt lgkmcnt(0)
	v_mfma_f32_16x16x128_f8f6f4 v[94:97], v[2:9], v[18:25], v[94:97]
	v_mfma_f32_16x16x128_f8f6f4 v[90:93], v[10:17], v[18:25], v[90:93]
	v_mfma_f32_16x16x128_f8f6f4 v[86:89], v[2:9], v[148:155], v[86:89]
	v_mfma_f32_16x16x128_f8f6f4 v[82:85], v[10:17], v[148:155], v[82:85]
	v_mfma_f32_16x16x128_f8f6f4 v[78:81], v[2:9], v[156:163], v[204:207]
	v_mfma_f32_16x16x128_f8f6f4 v[74:77], v[10:17], v[156:163], v[208:211]
	v_mfma_f32_16x16x128_f8f6f4 v[66:69], v[2:9], v[186:193], v[66:69]
	v_mfma_f32_16x16x128_f8f6f4 v[58:61], v[10:17], v[186:193], v[58:61]
	s_setprio 0
	s_setprio 1
	v_mfma_f32_16x16x128_f8f6f4 v[30:33], v[132:139], v[18:25], v[212:215]
	v_mfma_f32_16x16x128_f8f6f4 v[26:29], v[140:147], v[18:25], v[216:219]
	v_mfma_f32_16x16x128_f8f6f4 v[22:25], v[132:139], v[148:155], v[220:223]
	v_mfma_f32_16x16x128_f8f6f4 v[18:21], v[140:147], v[148:155], v[224:227]
	v_mfma_f32_16x16x128_f8f6f4 v[14:17], v[132:139], v[156:163], v[228:231]
	v_mfma_f32_16x16x128_f8f6f4 v[10:13], v[140:147], v[156:163], v[232:235]
	v_mfma_f32_16x16x128_f8f6f4 v[6:9], v[132:139], v[186:193], v[236:239]
	v_mfma_f32_16x16x128_f8f6f4 v[2:5], v[140:147], v[186:193], v[244:247]
	s_setprio 0
	s_barrier
	s_add_i32 s67, s67, 2
	s_add_u32 s65, s65, 0x100
	s_addc_u32 s66, s66, 0
	s_add_u32 s26, s26, 0x100
	s_addc_u32 s27, s27, 0
	s_cmp_gt_u32 s67, 5
	s_cbranch_scc0 .LBB0_1349
	s_and_b64 vcc, exec, s[8:9]
	s_cbranch_vccz .LBB0_1352
	s_barrier
